# Y8 expert-output stores in the down projection carry the nt cache hint; everything else identical to baseline
# speedup vs baseline: 1.0108x; 1.0040x over previous
; #define GAS __attribute__((address_space(1)))
; #define D2_STAGE(slot, J) do { _Pragma("unroll") for (int _h = 0; _h < 2; ++_h) _Pragma("unroll") for (int _i = 0; _i < 2; ++_i) \
;         __builtin_amdgcn_global_load_lds((const unsigned*)(wd + (size_t)(2 * (J) + _h) * (32 * 512) + goff[_i]), (LAS unsigned*)(c.lds + (slot) * 32768 + _h * 16384 + ldsw + _i * 8192), 16, 0, 0); } while (0)
; DI void phase_edown3(const Ctx& c, int layer) {
;     ...
;         if (wid == 0) {
;             unsigned sp = 0u;
;             while (fv < 2u) { fv = __hip_atomic_load(flags + (orow >> 8), __ATOMIC_RELAXED, __HIP_MEMORY_SCOPE_AGENT); if (fv >= 2u || ++sp > (1u << 18)) break; __builtin_amdgcn_s_sleep(8); }
;             __builtin_amdgcn_fence(__ATOMIC_ACQUIRE, "agent");
;             asm volatile("s_waitcnt vmcnt(0)" ::: "memory");
;         }
;         asm volatile("s_waitcnt lgkmcnt(0)" ::: "memory"); __builtin_amdgcn_s_barrier(); asm volatile("" ::: "memory");
;         bf16x8 afr[2][8];
; #pragma unroll
;         for (int mb = 0; mb < 2; ++mb)
; #pragma unroll
;             for (int ks = 0; ks < 8; ++ks) afr[mb][ks] = *(const GAS bf16x8*)(ACT + (size_t)(orow + 32 * wid + 16 * mb + fr) * 256 + ks * 32 + fq * 8);
;         if (wid == 0) {
;             const int pn2 = p + 256; fv = 0u;
;             if (pn2 < ntiles) { int tn; if (pn2 < 720) tn = (pn2 / 80) * 128 + 48 + pn2 % 80; else { const int q = pn2 - 720; tn = (q < 432) ? (q / 48) * 128 + q % 48 : 1152 + (q - 432); }
;                 fv = __hip_atomic_load(flags + (tn < nrt ? tn : (SH_BASE >> 8) + (tn - nrt)), __ATOMIC_RELAXED, __HIP_MEMORY_SCOPE_AGENT); }
;         }
;         D2_STAGE(0, 0);
;         bf16x8 bfr[8][2];
;         f32x4 acc[2][2];
; #pragma unroll
;         for (int mb = 0; mb < 2; ++mb)
; #pragma unroll
;             for (int nb = 0; nb < 2; ++nb) acc[mb][nb] = (f32x4){0.f, 0.f, 0.f, 0.f};
.LBB0_1282:
	s_add_i32 s18, s30, 0x2000
	s_mov_b32 m0, s30
	v_lshl_add_u64 v[72:73], s[16:17], 0, v[176:177]
	s_add_u32 s6, s16, 0x4000
	global_load_lds_dwordx4 v[72:73], off
	v_lshl_add_u64 v[72:73], s[16:17], 0, v[64:65]
	s_mov_b32 m0, s18
	s_addc_u32 s7, s17, 0
	s_add_i32 s19, s30, 0x4000
	global_load_lds_dwordx4 v[72:73], off
	v_lshl_add_u64 v[72:73], s[6:7], 0, v[176:177]
	s_mov_b32 m0, s19
	s_add_i32 s31, s30, 0x6000
	global_load_lds_dwordx4 v[72:73], off
	v_lshl_add_u64 v[72:73], s[6:7], 0, v[64:65]
	s_add_u32 s6, s16, 0x8000
	s_mov_b32 m0, s31
	s_addc_u32 s7, s17, 0
	s_add_i32 s36, s30, 0x8000
	global_load_lds_dwordx4 v[72:73], off
	v_lshl_add_u64 v[72:73], s[6:7], 0, v[176:177]
	s_mov_b32 m0, s36
	s_add_i32 s37, s30, 0xa000
	s_waitcnt vmcnt(0)
	s_waitcnt vmcnt(0)
	s_barrier
	global_load_lds_dwordx4 v[72:73], off
	v_lshl_add_u64 v[72:73], s[6:7], 0, v[64:65]
	s_add_u32 s6, s16, 0xc000
	s_mov_b32 m0, s37
	s_addc_u32 s7, s17, 0
	s_add_i32 s38, s30, 0xc000
	global_load_lds_dwordx4 v[72:73], off
	v_lshl_add_u64 v[72:73], s[6:7], 0, v[176:177]
	s_mov_b32 m0, s38
	s_add_i32 s39, s30, 0xe000
	global_load_lds_dwordx4 v[72:73], off
	v_lshl_add_u64 v[72:73], s[6:7], 0, v[64:65]
	s_mov_b32 m0, s39
	s_nop 0
	global_load_lds_dwordx4 v[72:73], off
	ds_read_b128 v[72:75], v94
	ds_read_b128 v[76:79], v94 offset:8192
	ds_read_b128 v[80:83], v95
	ds_read_b128 v[106:109], v95 offset:8192
	ds_read_b128 v[110:113], v96
	ds_read_b128 v[114:117], v96 offset:8192
	ds_read_b128 v[118:121], v97
	ds_read_b128 v[122:125], v97 offset:8192
	ds_read_b128 v[126:129], v98
	ds_read_b128 v[130:133], v98 offset:8192
	ds_read_b128 v[134:137], v99
	ds_read_b128 v[138:141], v99 offset:8192
	ds_read_b128 v[142:145], v100
	ds_read_b128 v[146:149], v100 offset:8192
	ds_read_b128 v[150:153], v101
	ds_read_b128 v[154:157], v101 offset:8192
	s_setprio 1
	s_waitcnt lgkmcnt(0)
	v_mfma_f32_16x16x32_bf16 v[158:161], v[72:75], v[0:3], 0
	v_mfma_f32_16x16x32_bf16 v[162:165], v[76:79], v[0:3], 0
	v_mfma_f32_16x16x32_bf16 v[72:75], v[72:75], v[32:35], 0
	v_mfma_f32_16x16x32_bf16 v[76:79], v[76:79], v[32:35], 0
	v_mfma_f32_16x16x32_bf16 v[162:165], v[106:109], v[4:7], v[162:165]
	v_mfma_f32_16x16x32_bf16 v[72:75], v[80:83], v[36:39], v[72:75]
	v_mfma_f32_16x16x32_bf16 v[76:79], v[106:109], v[36:39], v[76:79]
	v_mfma_f32_16x16x32_bf16 v[158:161], v[80:83], v[4:7], v[158:161]
	v_mfma_f32_16x16x32_bf16 v[106:109], v[114:117], v[8:11], v[162:165]
	v_mfma_f32_16x16x32_bf16 v[72:75], v[110:113], v[40:43], v[72:75]
	v_mfma_f32_16x16x32_bf16 v[76:79], v[114:117], v[40:43], v[76:79]
	v_mfma_f32_16x16x32_bf16 v[80:83], v[110:113], v[8:11], v[158:161]
	v_mfma_f32_16x16x32_bf16 v[106:109], v[122:125], v[12:15], v[106:109]
	v_mfma_f32_16x16x32_bf16 v[72:75], v[118:121], v[44:47], v[72:75]
	v_mfma_f32_16x16x32_bf16 v[76:79], v[122:125], v[44:47], v[76:79]
	v_mfma_f32_16x16x32_bf16 v[80:83], v[118:121], v[12:15], v[80:83]
	v_mfma_f32_16x16x32_bf16 v[106:109], v[130:133], v[16:19], v[106:109]
	v_mfma_f32_16x16x32_bf16 v[72:75], v[126:129], v[48:51], v[72:75]
	v_mfma_f32_16x16x32_bf16 v[76:79], v[130:133], v[48:51], v[76:79]
	v_mfma_f32_16x16x32_bf16 v[80:83], v[126:129], v[16:19], v[80:83]
	v_mfma_f32_16x16x32_bf16 v[106:109], v[138:141], v[20:23], v[106:109]
	v_mfma_f32_16x16x32_bf16 v[72:75], v[134:137], v[52:55], v[72:75]
	v_mfma_f32_16x16x32_bf16 v[76:79], v[138:141], v[52:55], v[76:79]
	v_mfma_f32_16x16x32_bf16 v[80:83], v[134:137], v[20:23], v[80:83]
	v_mfma_f32_16x16x32_bf16 v[106:109], v[146:149], v[24:27], v[106:109]
	v_mfma_f32_16x16x32_bf16 v[72:75], v[142:145], v[56:59], v[72:75]
	v_mfma_f32_16x16x32_bf16 v[76:79], v[146:149], v[56:59], v[76:79]
	v_mfma_f32_16x16x32_bf16 v[80:83], v[142:145], v[24:27], v[80:83]
	v_mfma_f32_16x16x32_bf16 v[106:109], v[154:157], v[28:31], v[106:109]
	v_mfma_f32_16x16x32_bf16 v[72:75], v[150:153], v[60:63], v[72:75]
	v_mfma_f32_16x16x32_bf16 v[76:79], v[154:157], v[60:63], v[76:79]
	v_mfma_f32_16x16x32_bf16 v[80:83], v[150:153], v[28:31], v[80:83]
	s_setprio 0
	s_nop 6
	v_max_f32_e64 v84, |v81|, |v81|
	v_max_f32_e64 v85, |v80|, |v80|
	v_max_f32_e32 v84, v85, v84
	v_max_f32_e64 v85, |v83|, |v83|
	v_max_f32_e64 v174, |v82|, |v82|
	v_max_f32_e32 v85, v174, v85
	v_max_f32_e64 v174, |v109|, |v109|
	v_max_f32_e64 v175, |v108|, |v108|
	v_max_f32_e32 v174, v175, v174
	v_max3_f32 v174, |v106|, |v107|, v174
	v_max3_f32 v84, v84, v85, v174
	v_mul_f32_e32 v84, 0x3c010204, v84
	v_lshrrev_b32_e32 v85, 23, v84
	v_and_b32_e32 v84, 0x7f800000, v84
	v_sub_u32_e32 v84, 0x7e800000, v84
	v_fmaak_f32 v80, v80, v84, 0x43000000
	v_cvt_pk_u8_f32 v80, v80, 0, 0
	v_fmaak_f32 v81, v81, v84, 0x43000000
	v_cvt_pk_u8_f32 v80, v81, 1, v80
	v_fmaak_f32 v81, v82, v84, 0x43000000
	v_cvt_pk_u8_f32 v80, v81, 2, v80
	v_fmaak_f32 v81, v83, v84, 0x43000000
	v_cvt_pk_u8_f32 v80, v81, 3, v80
	v_fmaak_f32 v81, v106, v84, 0x43000000
	v_cvt_pk_u8_f32 v81, v81, 0, 0
	v_fmaak_f32 v82, v107, v84, 0x43000000
	v_cvt_pk_u8_f32 v81, v82, 1, v81
	v_fmaak_f32 v82, v108, v84, 0x43000000
	v_cvt_pk_u8_f32 v81, v82, 2, v81
	v_fmaak_f32 v82, v109, v84, 0x43000000
	v_cvt_pk_u8_f32 v81, v82, 3, v81
	v_add_u16_e32 v82, 1, v85
	v_add_u32_e32 v106, v89, v86
	ds_read_b128 v[110:113], v94 offset:16384
	ds_read_b128 v[114:117], v94 offset:24576
	ds_read_b128 v[118:121], v95 offset:16384
	ds_read_b128 v[122:125], v95 offset:24576
	ds_read_b128 v[126:129], v96 offset:16384
	ds_read_b128 v[130:133], v96 offset:24576
	ds_read_b128 v[134:137], v97 offset:16384
	ds_read_b128 v[138:141], v97 offset:24576
	ds_read_b128 v[142:145], v98 offset:16384
	ds_read_b128 v[146:149], v98 offset:24576
	ds_read_b128 v[150:153], v99 offset:16384
	ds_read_b128 v[154:157], v99 offset:24576
	ds_read_b128 v[158:161], v100 offset:16384
	ds_read_b128 v[162:165], v100 offset:24576
	ds_read_b128 v[166:169], v101 offset:16384
	ds_read_b128 v[170:173], v101 offset:24576
	ds_write_b8 v106, v82 offset:128
	v_max_f32_e64 v82, |v73|, |v73|
	v_max_f32_e64 v83, |v72|, |v72|
	v_max_f32_e32 v82, v83, v82
	v_max_f32_e64 v83, |v75|, |v75|
	v_max_f32_e64 v84, |v74|, |v74|
	v_max_f32_e32 v83, v84, v83
	v_max_f32_e64 v84, |v79|, |v79|
	v_max_f32_e64 v85, |v78|, |v78|
	v_max_f32_e32 v84, v85, v84
	v_max3_f32 v84, |v76|, |v77|, v84
	v_max3_f32 v82, v82, v83, v84
	v_mul_f32_e32 v82, 0x3c010204, v82
	v_lshrrev_b32_e32 v83, 23, v82
	v_and_b32_e32 v82, 0x7f800000, v82
	v_sub_u32_e32 v82, 0x7e800000, v82
	v_fmaak_f32 v72, v72, v82, 0x43000000
	v_cvt_pk_u8_f32 v72, v72, 0, 0
	v_fmaak_f32 v73, v73, v82, 0x43000000
	v_cvt_pk_u8_f32 v72, v73, 1, v72
	v_fmaak_f32 v73, v74, v82, 0x43000000
	v_cvt_pk_u8_f32 v72, v73, 2, v72
	v_fmaak_f32 v73, v75, v82, 0x43000000
	v_cvt_pk_u8_f32 v72, v73, 3, v72
	v_fmaak_f32 v73, v76, v82, 0x43000000
	v_cvt_pk_u8_f32 v73, v73, 0, 0
	v_fmaak_f32 v74, v77, v82, 0x43000000
	v_cvt_pk_u8_f32 v73, v74, 1, v73
	v_fmaak_f32 v74, v78, v82, 0x43000000
	v_cvt_pk_u8_f32 v73, v74, 2, v73
	v_fmaak_f32 v74, v79, v82, 0x43000000
	v_cvt_pk_u8_f32 v73, v74, 3, v73
	ds_write2st64_b64 v102, v[80:81], v[72:73] offset1:5
	v_add_u16_e32 v72, 1, v83
	ds_write_b8 v106, v72 offset:2688
	s_setprio 1
	s_waitcnt lgkmcnt(0)
	v_mfma_f32_16x16x32_bf16 v[72:75], v[110:113], v[0:3], 0
	v_mfma_f32_16x16x32_bf16 v[76:79], v[114:117], v[0:3], 0
	v_mfma_f32_16x16x32_bf16 v[80:83], v[110:113], v[32:35], 0
	v_mfma_f32_16x16x32_bf16 v[108:111], v[114:117], v[32:35], 0
	v_mfma_f32_16x16x32_bf16 v[72:75], v[118:121], v[4:7], v[72:75]
	v_mfma_f32_16x16x32_bf16 v[76:79], v[122:125], v[4:7], v[76:79]
	v_mfma_f32_16x16x32_bf16 v[108:111], v[122:125], v[36:39], v[108:111]
	v_mfma_f32_16x16x32_bf16 v[80:83], v[118:121], v[36:39], v[80:83]
	v_mfma_f32_16x16x32_bf16 v[72:75], v[126:129], v[8:11], v[72:75]
	v_mfma_f32_16x16x32_bf16 v[76:79], v[130:133], v[8:11], v[76:79]
	v_mfma_f32_16x16x32_bf16 v[108:111], v[130:133], v[40:43], v[108:111]
	v_mfma_f32_16x16x32_bf16 v[80:83], v[126:129], v[40:43], v[80:83]
	v_mfma_f32_16x16x32_bf16 v[72:75], v[134:137], v[12:15], v[72:75]
	v_mfma_f32_16x16x32_bf16 v[76:79], v[138:141], v[12:15], v[76:79]
	v_mfma_f32_16x16x32_bf16 v[108:111], v[138:141], v[44:47], v[108:111]
	v_mfma_f32_16x16x32_bf16 v[80:83], v[134:137], v[44:47], v[80:83]
	v_mfma_f32_16x16x32_bf16 v[72:75], v[142:145], v[16:19], v[72:75]
	v_mfma_f32_16x16x32_bf16 v[76:79], v[146:149], v[16:19], v[76:79]
	v_mfma_f32_16x16x32_bf16 v[108:111], v[146:149], v[48:51], v[108:111]
	v_mfma_f32_16x16x32_bf16 v[80:83], v[142:145], v[48:51], v[80:83]
	v_mfma_f32_16x16x32_bf16 v[72:75], v[150:153], v[20:23], v[72:75]
	v_mfma_f32_16x16x32_bf16 v[76:79], v[154:157], v[20:23], v[76:79]
	v_mfma_f32_16x16x32_bf16 v[108:111], v[154:157], v[52:55], v[108:111]
	v_mfma_f32_16x16x32_bf16 v[80:83], v[150:153], v[52:55], v[80:83]
	v_mfma_f32_16x16x32_bf16 v[72:75], v[158:161], v[24:27], v[72:75]
	v_mfma_f32_16x16x32_bf16 v[76:79], v[162:165], v[24:27], v[76:79]
	v_mfma_f32_16x16x32_bf16 v[108:111], v[162:165], v[56:59], v[108:111]
	v_mfma_f32_16x16x32_bf16 v[80:83], v[158:161], v[56:59], v[80:83]
	v_mfma_f32_16x16x32_bf16 v[72:75], v[166:169], v[28:31], v[72:75]
	v_mfma_f32_16x16x32_bf16 v[76:79], v[170:173], v[28:31], v[76:79]
	v_mfma_f32_16x16x32_bf16 v[108:111], v[170:173], v[60:63], v[108:111]
	v_mfma_f32_16x16x32_bf16 v[80:83], v[166:169], v[60:63], v[80:83]
	s_setprio 0
	s_nop 3
	v_max_f32_e64 v84, |v73|, |v73|
	v_max_f32_e64 v85, |v72|, |v72|
	v_max_f32_e32 v84, v85, v84
	v_max_f32_e64 v85, |v75|, |v75|
	v_max_f32_e64 v107, |v74|, |v74|
	v_max_f32_e32 v85, v107, v85
	v_max_f32_e64 v107, |v79|, |v79|
	v_max_f32_e64 v112, |v78|, |v78|
	v_max_f32_e32 v107, v112, v107
	v_max3_f32 v107, |v76|, |v77|, v107
	v_max3_f32 v84, v84, v85, v107
	v_mul_f32_e32 v84, 0x3c010204, v84
	v_lshrrev_b32_e32 v85, 23, v84
	v_and_b32_e32 v84, 0x7f800000, v84
	v_sub_u32_e32 v84, 0x7e800000, v84
	v_fmaak_f32 v72, v72, v84, 0x43000000
	v_cvt_pk_u8_f32 v72, v72, 0, 0
	v_fmaak_f32 v73, v73, v84, 0x43000000
	v_cvt_pk_u8_f32 v72, v73, 1, v72
	v_fmaak_f32 v73, v74, v84, 0x43000000
	v_cvt_pk_u8_f32 v72, v73, 2, v72
	v_fmaak_f32 v73, v75, v84, 0x43000000
	v_cvt_pk_u8_f32 v72, v73, 3, v72
	v_fmaak_f32 v73, v76, v84, 0x43000000
	v_cvt_pk_u8_f32 v73, v73, 0, 0
	v_fmaak_f32 v74, v77, v84, 0x43000000
	v_cvt_pk_u8_f32 v73, v74, 1, v73
	v_fmaak_f32 v74, v78, v84, 0x43000000
	v_cvt_pk_u8_f32 v73, v74, 2, v73
	v_fmaak_f32 v74, v79, v84, 0x43000000
	v_cvt_pk_u8_f32 v73, v74, 3, v73
	v_add_u16_e32 v74, 1, v85
	ds_write_b8 v106, v74 offset:132
	v_max_f32_e64 v74, |v81|, |v81|
	v_max_f32_e64 v75, |v80|, |v80|
	v_max_f32_e32 v74, v75, v74
	v_max_f32_e64 v75, |v83|, |v83|
	v_max_f32_e64 v76, |v82|, |v82|
	v_max_f32_e32 v75, v76, v75
	v_max_f32_e64 v76, |v111|, |v111|
	v_max_f32_e64 v77, |v110|, |v110|
	v_max_f32_e32 v76, v77, v76
	v_max3_f32 v76, |v108|, |v109|, v76
	v_max3_f32 v74, v74, v75, v76
	v_mul_f32_e32 v74, 0x3c010204, v74
	v_lshrrev_b32_e32 v76, 23, v74
	v_and_b32_e32 v74, 0x7f800000, v74
	v_sub_u32_e32 v75, 0x7e800000, v74
	v_fmaak_f32 v74, v80, v75, 0x43000000
	v_cvt_pk_u8_f32 v74, v74, 0, 0
	v_fmaak_f32 v77, v81, v75, 0x43000000
	v_cvt_pk_u8_f32 v74, v77, 1, v74
	v_fmaak_f32 v77, v82, v75, 0x43000000
	v_cvt_pk_u8_f32 v74, v77, 2, v74
	v_fmaak_f32 v77, v83, v75, 0x43000000
	v_cvt_pk_u8_f32 v74, v77, 3, v74
	v_fmaak_f32 v77, v108, v75, 0x43000000
	v_cvt_pk_u8_f32 v77, v77, 0, 0
	v_fmaak_f32 v78, v109, v75, 0x43000000
	v_cvt_pk_u8_f32 v77, v78, 1, v77
	v_fmaak_f32 v78, v110, v75, 0x43000000
	v_cvt_pk_u8_f32 v77, v78, 2, v77
	v_fmaak_f32 v75, v111, v75, 0x43000000
	v_cvt_pk_u8_f32 v75, v75, 3, v77
	v_add_u32_e32 v107, 32, v102
	s_add_u32 s6, s16, 0x10000
	ds_write2st64_b64 v107, v[72:73], v[74:75] offset1:5
	v_add_u16_e32 v72, 1, v76
	s_addc_u32 s7, s17, 0
	s_mov_b32 m0, s30
	ds_write_b8 v106, v72 offset:2692
	v_lshl_add_u64 v[72:73], s[6:7], 0, v[176:177]
	s_waitcnt vmcnt(0)
	s_barrier
	global_load_lds_dwordx4 v[72:73], off
	v_lshl_add_u64 v[72:73], s[6:7], 0, v[64:65]
	s_add_u32 s6, s16, 0x14000
	s_mov_b32 m0, s18
	s_addc_u32 s7, s17, 0
	global_load_lds_dwordx4 v[72:73], off
	v_lshl_add_u64 v[72:73], s[6:7], 0, v[176:177]
	s_mov_b32 m0, s19
	s_nop 0
	global_load_lds_dwordx4 v[72:73], off
	v_lshl_add_u64 v[72:73], s[6:7], 0, v[64:65]
	s_mov_b32 m0, s31
	s_nop 0
	global_load_lds_dwordx4 v[72:73], off
	ds_read_b128 v[72:75], v94 offset:32768
	ds_read_b128 v[76:79], v94 offset:40960
	ds_read_b128 v[80:83], v95 offset:32768
	ds_read_b128 v[108:111], v95 offset:40960
	ds_read_b128 v[112:115], v96 offset:32768
	ds_read_b128 v[116:119], v96 offset:40960
	ds_read_b128 v[120:123], v97 offset:32768
	ds_read_b128 v[124:127], v97 offset:40960
	ds_read_b128 v[128:131], v98 offset:32768
	ds_read_b128 v[132:135], v98 offset:40960
	ds_read_b128 v[136:139], v99 offset:32768
	ds_read_b128 v[140:143], v99 offset:40960
	ds_read_b128 v[144:147], v100 offset:32768
	ds_read_b128 v[148:151], v100 offset:40960
	ds_read_b128 v[152:155], v101 offset:32768
	ds_read_b128 v[156:159], v101 offset:40960
	s_setprio 1
	s_waitcnt lgkmcnt(0)
	v_mfma_f32_16x16x32_bf16 v[160:163], v[72:75], v[0:3], 0
	v_mfma_f32_16x16x32_bf16 v[164:167], v[76:79], v[0:3], 0
	v_mfma_f32_16x16x32_bf16 v[72:75], v[72:75], v[32:35], 0
	v_mfma_f32_16x16x32_bf16 v[76:79], v[76:79], v[32:35], 0
	v_mfma_f32_16x16x32_bf16 v[164:167], v[108:111], v[4:7], v[164:167]
	v_mfma_f32_16x16x32_bf16 v[72:75], v[80:83], v[36:39], v[72:75]
	v_mfma_f32_16x16x32_bf16 v[76:79], v[108:111], v[36:39], v[76:79]
	v_mfma_f32_16x16x32_bf16 v[160:163], v[80:83], v[4:7], v[160:163]
	v_mfma_f32_16x16x32_bf16 v[108:111], v[116:119], v[8:11], v[164:167]
	v_mfma_f32_16x16x32_bf16 v[72:75], v[112:115], v[40:43], v[72:75]
	v_mfma_f32_16x16x32_bf16 v[76:79], v[116:119], v[40:43], v[76:79]
	v_mfma_f32_16x16x32_bf16 v[80:83], v[112:115], v[8:11], v[160:163]
	v_mfma_f32_16x16x32_bf16 v[108:111], v[124:127], v[12:15], v[108:111]
	v_mfma_f32_16x16x32_bf16 v[72:75], v[120:123], v[44:47], v[72:75]
	v_mfma_f32_16x16x32_bf16 v[76:79], v[124:127], v[44:47], v[76:79]
	v_mfma_f32_16x16x32_bf16 v[80:83], v[120:123], v[12:15], v[80:83]
	v_mfma_f32_16x16x32_bf16 v[108:111], v[132:135], v[16:19], v[108:111]
	v_mfma_f32_16x16x32_bf16 v[72:75], v[128:131], v[48:51], v[72:75]
	v_mfma_f32_16x16x32_bf16 v[76:79], v[132:135], v[48:51], v[76:79]
	v_mfma_f32_16x16x32_bf16 v[80:83], v[128:131], v[16:19], v[80:83]
	v_mfma_f32_16x16x32_bf16 v[108:111], v[140:143], v[20:23], v[108:111]
	v_mfma_f32_16x16x32_bf16 v[72:75], v[136:139], v[52:55], v[72:75]
	v_mfma_f32_16x16x32_bf16 v[76:79], v[140:143], v[52:55], v[76:79]
	v_mfma_f32_16x16x32_bf16 v[80:83], v[136:139], v[20:23], v[80:83]
	v_mfma_f32_16x16x32_bf16 v[108:111], v[148:151], v[24:27], v[108:111]
	v_mfma_f32_16x16x32_bf16 v[72:75], v[144:147], v[56:59], v[72:75]
	v_mfma_f32_16x16x32_bf16 v[76:79], v[148:151], v[56:59], v[76:79]
	v_mfma_f32_16x16x32_bf16 v[80:83], v[144:147], v[24:27], v[80:83]
	v_mfma_f32_16x16x32_bf16 v[108:111], v[156:159], v[28:31], v[108:111]
	v_mfma_f32_16x16x32_bf16 v[72:75], v[152:155], v[60:63], v[72:75]
	v_mfma_f32_16x16x32_bf16 v[76:79], v[156:159], v[60:63], v[76:79]
	v_mfma_f32_16x16x32_bf16 v[80:83], v[152:155], v[28:31], v[80:83]
	s_setprio 0
	s_nop 6
	v_max_f32_e64 v84, |v81|, |v81|
	v_max_f32_e64 v85, |v80|, |v80|
	v_max_f32_e32 v84, v85, v84
	v_max_f32_e64 v85, |v83|, |v83|
	v_max_f32_e64 v178, |v82|, |v82|
	v_max_f32_e32 v85, v178, v85
	v_max_f32_e64 v178, |v111|, |v111|
	v_max_f32_e64 v179, |v110|, |v110|
	v_max_f32_e32 v178, v179, v178
	v_max3_f32 v178, |v108|, |v109|, v178
	v_max3_f32 v84, v84, v85, v178
	v_mul_f32_e32 v84, 0x3c010204, v84
	v_lshrrev_b32_e32 v85, 23, v84
	v_and_b32_e32 v84, 0x7f800000, v84
	v_sub_u32_e32 v84, 0x7e800000, v84
	v_fmaak_f32 v80, v80, v84, 0x43000000
	v_cvt_pk_u8_f32 v80, v80, 0, 0
	v_fmaak_f32 v81, v81, v84, 0x43000000
	v_cvt_pk_u8_f32 v80, v81, 1, v80
	v_fmaak_f32 v81, v82, v84, 0x43000000
	v_cvt_pk_u8_f32 v80, v81, 2, v80
	v_fmaak_f32 v81, v83, v84, 0x43000000
	v_cvt_pk_u8_f32 v80, v81, 3, v80
	v_fmaak_f32 v81, v108, v84, 0x43000000
	v_cvt_pk_u8_f32 v81, v81, 0, 0
	v_fmaak_f32 v82, v109, v84, 0x43000000
	v_cvt_pk_u8_f32 v81, v82, 1, v81
	v_fmaak_f32 v82, v110, v84, 0x43000000
	v_cvt_pk_u8_f32 v81, v82, 2, v81
	v_fmaak_f32 v82, v111, v84, 0x43000000
	v_cvt_pk_u8_f32 v81, v82, 3, v81
	v_add_u16_e32 v82, 1, v85
	ds_read_b128 v[112:115], v94 offset:49152
	ds_read_b128 v[116:119], v94 offset:57344
	ds_read_b128 v[120:123], v95 offset:49152
	ds_read_b128 v[124:127], v95 offset:57344
	ds_read_b128 v[128:131], v96 offset:49152
	ds_read_b128 v[132:135], v96 offset:57344
	ds_read_b128 v[136:139], v97 offset:49152
	ds_read_b128 v[140:143], v97 offset:57344
	ds_read_b128 v[144:147], v98 offset:49152
	ds_read_b128 v[148:151], v98 offset:57344
	ds_read_b128 v[152:155], v99 offset:49152
	ds_read_b128 v[156:159], v99 offset:57344
	ds_read_b128 v[160:163], v100 offset:49152
	ds_read_b128 v[164:167], v100 offset:57344
	ds_read_b128 v[168:171], v101 offset:49152
	ds_read_b128 v[172:175], v101 offset:57344
	ds_write_b8 v106, v82 offset:136
	v_max_f32_e64 v82, |v73|, |v73|
	v_max_f32_e64 v83, |v72|, |v72|
	v_max_f32_e32 v82, v83, v82
	v_max_f32_e64 v83, |v75|, |v75|
	v_max_f32_e64 v84, |v74|, |v74|
	v_max_f32_e32 v83, v84, v83
	v_max_f32_e64 v84, |v79|, |v79|
	v_max_f32_e64 v85, |v78|, |v78|
	v_max_f32_e32 v84, v85, v84
	v_max3_f32 v84, |v76|, |v77|, v84
	v_max3_f32 v82, v82, v83, v84
	v_mul_f32_e32 v82, 0x3c010204, v82
	v_lshrrev_b32_e32 v83, 23, v82
	v_and_b32_e32 v82, 0x7f800000, v82
	v_sub_u32_e32 v82, 0x7e800000, v82
	v_fmaak_f32 v72, v72, v82, 0x43000000
	v_cvt_pk_u8_f32 v72, v72, 0, 0
	v_fmaak_f32 v73, v73, v82, 0x43000000
	v_cvt_pk_u8_f32 v72, v73, 1, v72
	v_fmaak_f32 v73, v74, v82, 0x43000000
	v_cvt_pk_u8_f32 v72, v73, 2, v72
	v_fmaak_f32 v73, v75, v82, 0x43000000
	v_cvt_pk_u8_f32 v72, v73, 3, v72
	v_fmaak_f32 v73, v76, v82, 0x43000000
	v_cvt_pk_u8_f32 v73, v73, 0, 0
	v_fmaak_f32 v74, v77, v82, 0x43000000
	v_cvt_pk_u8_f32 v73, v74, 1, v73
	v_fmaak_f32 v74, v78, v82, 0x43000000
	v_cvt_pk_u8_f32 v73, v74, 2, v73
	v_fmaak_f32 v74, v79, v82, 0x43000000
	v_cvt_pk_u8_f32 v73, v74, 3, v73
	v_add_u32_e32 v108, 64, v102
	ds_write2st64_b64 v108, v[80:81], v[72:73] offset1:5
	v_add_u16_e32 v72, 1, v83
	ds_write_b8 v106, v72 offset:2696
	s_setprio 1
	s_waitcnt lgkmcnt(0)
	v_mfma_f32_16x16x32_bf16 v[72:75], v[112:115], v[0:3], 0
	v_mfma_f32_16x16x32_bf16 v[76:79], v[116:119], v[0:3], 0
	v_mfma_f32_16x16x32_bf16 v[80:83], v[112:115], v[32:35], 0
	v_mfma_f32_16x16x32_bf16 v[110:113], v[116:119], v[32:35], 0
	v_mfma_f32_16x16x32_bf16 v[72:75], v[120:123], v[4:7], v[72:75]
	v_mfma_f32_16x16x32_bf16 v[76:79], v[124:127], v[4:7], v[76:79]
	v_mfma_f32_16x16x32_bf16 v[80:83], v[120:123], v[36:39], v[80:83]
	v_mfma_f32_16x16x32_bf16 v[110:113], v[124:127], v[36:39], v[110:113]
	v_mfma_f32_16x16x32_bf16 v[72:75], v[128:131], v[8:11], v[72:75]
	v_mfma_f32_16x16x32_bf16 v[76:79], v[132:135], v[8:11], v[76:79]
	v_mfma_f32_16x16x32_bf16 v[80:83], v[128:131], v[40:43], v[80:83]
	v_mfma_f32_16x16x32_bf16 v[110:113], v[132:135], v[40:43], v[110:113]
	v_mfma_f32_16x16x32_bf16 v[72:75], v[136:139], v[12:15], v[72:75]
	v_mfma_f32_16x16x32_bf16 v[76:79], v[140:143], v[12:15], v[76:79]
	v_mfma_f32_16x16x32_bf16 v[80:83], v[136:139], v[44:47], v[80:83]
	v_mfma_f32_16x16x32_bf16 v[110:113], v[140:143], v[44:47], v[110:113]
	v_mfma_f32_16x16x32_bf16 v[72:75], v[144:147], v[16:19], v[72:75]
	v_mfma_f32_16x16x32_bf16 v[76:79], v[148:151], v[16:19], v[76:79]
	v_mfma_f32_16x16x32_bf16 v[80:83], v[144:147], v[48:51], v[80:83]
	v_mfma_f32_16x16x32_bf16 v[110:113], v[148:151], v[48:51], v[110:113]
	v_mfma_f32_16x16x32_bf16 v[72:75], v[152:155], v[20:23], v[72:75]
	v_mfma_f32_16x16x32_bf16 v[76:79], v[156:159], v[20:23], v[76:79]
	v_mfma_f32_16x16x32_bf16 v[80:83], v[152:155], v[52:55], v[80:83]
	v_mfma_f32_16x16x32_bf16 v[110:113], v[156:159], v[52:55], v[110:113]
	v_mfma_f32_16x16x32_bf16 v[72:75], v[160:163], v[24:27], v[72:75]
	v_mfma_f32_16x16x32_bf16 v[76:79], v[164:167], v[24:27], v[76:79]
	v_mfma_f32_16x16x32_bf16 v[80:83], v[160:163], v[56:59], v[80:83]
	v_mfma_f32_16x16x32_bf16 v[110:113], v[164:167], v[56:59], v[110:113]
	v_mfma_f32_16x16x32_bf16 v[72:75], v[168:171], v[28:31], v[72:75]
	v_mfma_f32_16x16x32_bf16 v[76:79], v[172:175], v[28:31], v[76:79]
	v_mfma_f32_16x16x32_bf16 v[80:83], v[168:171], v[60:63], v[80:83]
	v_mfma_f32_16x16x32_bf16 v[110:113], v[172:175], v[60:63], v[110:113]
	s_setprio 0
	s_nop 3
	v_max_f32_e64 v84, |v73|, |v73|
	v_max_f32_e64 v85, |v72|, |v72|
	v_max_f32_e32 v84, v85, v84
	v_max_f32_e64 v85, |v75|, |v75|
	v_max_f32_e64 v109, |v74|, |v74|
	v_max_f32_e32 v85, v109, v85
	v_max_f32_e64 v109, |v79|, |v79|
	v_max_f32_e64 v114, |v78|, |v78|
	v_max_f32_e32 v109, v114, v109
	v_max3_f32 v109, |v76|, |v77|, v109
	v_max3_f32 v84, v84, v85, v109
	v_mul_f32_e32 v84, 0x3c010204, v84
	v_lshrrev_b32_e32 v85, 23, v84
	v_and_b32_e32 v84, 0x7f800000, v84
	v_sub_u32_e32 v84, 0x7e800000, v84
	v_fmaak_f32 v72, v72, v84, 0x43000000
	v_cvt_pk_u8_f32 v72, v72, 0, 0
	v_fmaak_f32 v73, v73, v84, 0x43000000
	v_cvt_pk_u8_f32 v72, v73, 1, v72
	v_fmaak_f32 v73, v74, v84, 0x43000000
	v_cvt_pk_u8_f32 v72, v73, 2, v72
	v_fmaak_f32 v73, v75, v84, 0x43000000
	v_cvt_pk_u8_f32 v72, v73, 3, v72
	v_fmaak_f32 v73, v76, v84, 0x43000000
	v_cvt_pk_u8_f32 v73, v73, 0, 0
	v_fmaak_f32 v74, v77, v84, 0x43000000
	v_cvt_pk_u8_f32 v73, v74, 1, v73
	v_fmaak_f32 v74, v78, v84, 0x43000000
	v_cvt_pk_u8_f32 v73, v74, 2, v73
	v_fmaak_f32 v74, v79, v84, 0x43000000
	v_cvt_pk_u8_f32 v73, v74, 3, v73
	v_add_u16_e32 v74, 1, v85
	ds_write_b8 v106, v74 offset:140
	v_max_f32_e64 v74, |v81|, |v81|
	v_max_f32_e64 v75, |v80|, |v80|
	v_max_f32_e32 v74, v75, v74
	v_max_f32_e64 v75, |v83|, |v83|
	v_max_f32_e64 v76, |v82|, |v82|
	v_max_f32_e32 v75, v76, v75
	v_max_f32_e64 v76, |v113|, |v113|
	v_max_f32_e64 v77, |v112|, |v112|
	v_max_f32_e32 v76, v77, v76
	v_max3_f32 v76, |v110|, |v111|, v76
	v_max3_f32 v74, v74, v75, v76
	v_mul_f32_e32 v74, 0x3c010204, v74
	v_lshrrev_b32_e32 v76, 23, v74
	v_and_b32_e32 v74, 0x7f800000, v74
	v_sub_u32_e32 v75, 0x7e800000, v74
	v_fmaak_f32 v74, v80, v75, 0x43000000
	v_cvt_pk_u8_f32 v74, v74, 0, 0
	v_fmaak_f32 v77, v81, v75, 0x43000000
	v_cvt_pk_u8_f32 v74, v77, 1, v74
	v_fmaak_f32 v77, v82, v75, 0x43000000
	v_cvt_pk_u8_f32 v74, v77, 2, v74
	v_fmaak_f32 v77, v83, v75, 0x43000000
	v_cvt_pk_u8_f32 v74, v77, 3, v74
	v_fmaak_f32 v77, v110, v75, 0x43000000
	v_cvt_pk_u8_f32 v77, v77, 0, 0
	v_fmaak_f32 v78, v111, v75, 0x43000000
	v_cvt_pk_u8_f32 v77, v78, 1, v77
	v_fmaak_f32 v78, v112, v75, 0x43000000
	v_cvt_pk_u8_f32 v77, v78, 2, v77
	v_fmaak_f32 v75, v113, v75, 0x43000000
	v_cvt_pk_u8_f32 v75, v75, 3, v77
	v_add_u32_e32 v109, 0x60, v102
	ds_write2st64_b64 v109, v[72:73], v[74:75] offset1:5
	v_add_u16_e32 v72, 1, v76
	ds_write_b8 v106, v72 offset:2700
	ds_read_b128 v[76:79], v103
	ds_read_b128 v[80:83], v103 offset:1280
	s_add_i32 s8, s40, s29
	v_add_u32_e32 v74, s8, v90
	v_mad_i64_i32 v[72:73], s[6:7], v74, s50, v[68:69]
	v_add_u32_e32 v75, s8, v91
	s_waitcnt lgkmcnt(0)
	global_store_dwordx4 v[72:73], v[76:79], off nt
	v_mad_i64_i32 v[72:73], s[6:7], v75, s50, v[68:69]
	global_store_dwordx4 v[72:73], v[80:83], off nt
	ds_read_b128 v[78:81], v103 offset:2560
	ds_read_b128 v[82:85], v103 offset:3840
	v_add_u32_e32 v76, s8, v92
	v_mad_i64_i32 v[72:73], s[6:7], v76, s50, v[68:69]
	v_add_u32_e32 v77, s8, v93
	s_waitcnt lgkmcnt(0)
	global_store_dwordx4 v[72:73], v[78:81], off nt
	v_mad_i64_i32 v[72:73], s[6:7], v77, s50, v[68:69]
	s_nop 0
	v_add_u32_e32 v78, s40, v88
	global_store_dwordx4 v[72:73], v[82:85], off nt
	s_and_saveexec_b64 s[6:7], s[4:5]
	s_xor_b64 s[6:7], exec, s[6:7]
	v_mad_i64_i32 v[72:73], s[8:9], v78, s50, 0
	s_andn2_saveexec_b64 s[6:7], s[6:7]
	s_cbranch_execz .LBB0_1286
	ds_read_b128 v[80:83], v104 offset:128
	v_mov_b64_e32 v[84:85], s[10:11]
	v_mad_i64_i32 v[72:73], s[8:9], v78, s50, 0
	v_mad_i64_i32 v[78:79], s[8:9], v78, s50, v[84:85]
	s_waitcnt lgkmcnt(0)
	global_store_dwordx4 v[78:79], v[80:83], off offset:1024 nt

.LBB0_1290:
	ds_read_b128 v[82:85], v94 offset:32768
	ds_read_b128 v[110:113], v94 offset:40960
	ds_read_b128 v[114:117], v95 offset:32768
	ds_read_b128 v[118:121], v95 offset:40960
	ds_read_b128 v[122:125], v96 offset:32768
	ds_read_b128 v[126:129], v96 offset:40960
	ds_read_b128 v[130:133], v97 offset:32768
	ds_read_b128 v[134:137], v97 offset:40960
	ds_read_b128 v[138:141], v98 offset:32768
	ds_read_b128 v[142:145], v98 offset:40960
	ds_read_b128 v[146:149], v99 offset:32768
	ds_read_b128 v[150:153], v99 offset:40960
	ds_read_b128 v[154:157], v100 offset:32768
	ds_read_b128 v[158:161], v100 offset:40960
	ds_read_b128 v[162:165], v101 offset:32768
	ds_read_b128 v[166:169], v101 offset:40960
	s_setprio 1
	s_waitcnt lgkmcnt(0)
	v_mfma_f32_16x16x32_bf16 v[170:173], v[82:85], v[0:3], 0
	v_mfma_f32_16x16x32_bf16 v[178:181], v[110:113], v[0:3], 0
	v_mfma_f32_16x16x32_bf16 v[82:85], v[82:85], v[32:35], 0
	v_mfma_f32_16x16x32_bf16 v[110:113], v[110:113], v[32:35], 0
	v_mfma_f32_16x16x32_bf16 v[170:173], v[114:117], v[4:7], v[170:173]
	v_mfma_f32_16x16x32_bf16 v[178:181], v[118:121], v[4:7], v[178:181]
	v_mfma_f32_16x16x32_bf16 v[82:85], v[114:117], v[36:39], v[82:85]
	v_mfma_f32_16x16x32_bf16 v[110:113], v[118:121], v[36:39], v[110:113]
	v_mfma_f32_16x16x32_bf16 v[114:117], v[122:125], v[8:11], v[170:173]
	v_mfma_f32_16x16x32_bf16 v[118:121], v[126:129], v[8:11], v[178:181]
	v_mfma_f32_16x16x32_bf16 v[82:85], v[122:125], v[40:43], v[82:85]
	v_mfma_f32_16x16x32_bf16 v[110:113], v[126:129], v[40:43], v[110:113]
	v_mfma_f32_16x16x32_bf16 v[114:117], v[130:133], v[12:15], v[114:117]
	v_mfma_f32_16x16x32_bf16 v[118:121], v[134:137], v[12:15], v[118:121]
	v_mfma_f32_16x16x32_bf16 v[82:85], v[130:133], v[44:47], v[82:85]
	v_mfma_f32_16x16x32_bf16 v[110:113], v[134:137], v[44:47], v[110:113]
	v_mfma_f32_16x16x32_bf16 v[114:117], v[138:141], v[16:19], v[114:117]
	v_mfma_f32_16x16x32_bf16 v[118:121], v[142:145], v[16:19], v[118:121]
	v_mfma_f32_16x16x32_bf16 v[82:85], v[138:141], v[48:51], v[82:85]
	v_mfma_f32_16x16x32_bf16 v[110:113], v[142:145], v[48:51], v[110:113]
	v_mfma_f32_16x16x32_bf16 v[114:117], v[146:149], v[20:23], v[114:117]
	v_mfma_f32_16x16x32_bf16 v[118:121], v[150:153], v[20:23], v[118:121]
	v_mfma_f32_16x16x32_bf16 v[82:85], v[146:149], v[52:55], v[82:85]
	v_mfma_f32_16x16x32_bf16 v[110:113], v[150:153], v[52:55], v[110:113]
	v_mfma_f32_16x16x32_bf16 v[114:117], v[154:157], v[24:27], v[114:117]
	v_mfma_f32_16x16x32_bf16 v[118:121], v[158:161], v[24:27], v[118:121]
	v_mfma_f32_16x16x32_bf16 v[82:85], v[154:157], v[56:59], v[82:85]
	v_mfma_f32_16x16x32_bf16 v[110:113], v[158:161], v[56:59], v[110:113]
	v_mfma_f32_16x16x32_bf16 v[114:117], v[162:165], v[28:31], v[114:117]
	v_mfma_f32_16x16x32_bf16 v[118:121], v[166:169], v[28:31], v[118:121]
	v_mfma_f32_16x16x32_bf16 v[82:85], v[162:165], v[60:63], v[82:85]
	v_mfma_f32_16x16x32_bf16 v[110:113], v[166:169], v[60:63], v[110:113]
	s_setprio 0
	s_nop 3
	v_max_f32_e64 v174, |v115|, |v115|
	v_max_f32_e64 v175, |v114|, |v114|
	v_max_f32_e32 v174, v175, v174
	v_max_f32_e64 v175, |v117|, |v117|
	v_max_f32_e64 v190, |v116|, |v116|
	v_max_f32_e32 v175, v190, v175
	v_max_f32_e64 v190, |v121|, |v121|
	v_max_f32_e64 v191, |v120|, |v120|
	v_max_f32_e32 v190, v191, v190
	v_max3_f32 v190, |v118|, |v119|, v190
	v_max3_f32 v174, v174, v175, v190
	v_mul_f32_e32 v174, 0x3c010204, v174
	v_lshrrev_b32_e32 v175, 23, v174
	v_and_b32_e32 v174, 0x7f800000, v174
	v_sub_u32_e32 v174, 0x7e800000, v174
	v_fmaak_f32 v114, v114, v174, 0x43000000
	v_cvt_pk_u8_f32 v114, v114, 0, 0
	v_fmaak_f32 v115, v115, v174, 0x43000000
	v_cvt_pk_u8_f32 v114, v115, 1, v114
	v_fmaak_f32 v115, v116, v174, 0x43000000
	v_cvt_pk_u8_f32 v114, v115, 2, v114
	v_fmaak_f32 v115, v117, v174, 0x43000000
	v_cvt_pk_u8_f32 v114, v115, 3, v114
	v_fmaak_f32 v115, v118, v174, 0x43000000
	v_cvt_pk_u8_f32 v115, v115, 0, 0
	v_fmaak_f32 v116, v119, v174, 0x43000000
	v_cvt_pk_u8_f32 v115, v116, 1, v115
	v_fmaak_f32 v116, v120, v174, 0x43000000
	v_cvt_pk_u8_f32 v115, v116, 2, v115
	v_fmaak_f32 v116, v121, v174, 0x43000000
	v_cvt_pk_u8_f32 v115, v116, 3, v115
	v_add_u16_e32 v116, 1, v175
	ds_read_b128 v[122:125], v94 offset:49152
	ds_read_b128 v[126:129], v94 offset:57344
	ds_read_b128 v[130:133], v95 offset:49152
	ds_read_b128 v[134:137], v95 offset:57344
	ds_read_b128 v[138:141], v96 offset:49152
	ds_read_b128 v[142:145], v96 offset:57344
	ds_read_b128 v[146:149], v97 offset:49152
	ds_read_b128 v[150:153], v97 offset:57344
	ds_read_b128 v[154:157], v98 offset:49152
	ds_read_b128 v[158:161], v98 offset:57344
	ds_read_b128 v[162:165], v99 offset:49152
	ds_read_b128 v[166:169], v99 offset:57344
	ds_read_b128 v[170:173], v100 offset:49152
	ds_read_b128 v[178:181], v100 offset:57344
	ds_read_b128 v[182:185], v101 offset:49152
	ds_read_b128 v[186:189], v101 offset:57344
	ds_write_b8 v106, v116 offset:136
	v_max_f32_e64 v116, |v83|, |v83|
	v_max_f32_e64 v117, |v82|, |v82|
	v_max_f32_e32 v116, v117, v116
	v_max_f32_e64 v117, |v85|, |v85|
	v_max_f32_e64 v118, |v84|, |v84|
	v_max_f32_e32 v117, v118, v117
	v_max_f32_e64 v118, |v113|, |v113|
	v_max_f32_e64 v119, |v112|, |v112|
	v_max_f32_e32 v118, v119, v118
	v_max3_f32 v118, |v110|, |v111|, v118
	v_max3_f32 v116, v116, v117, v118
	v_mul_f32_e32 v116, 0x3c010204, v116
	v_lshrrev_b32_e32 v117, 23, v116
	v_and_b32_e32 v116, 0x7f800000, v116
	v_sub_u32_e32 v116, 0x7e800000, v116
	v_fmaak_f32 v82, v82, v116, 0x43000000
	v_cvt_pk_u8_f32 v82, v82, 0, 0
	v_fmaak_f32 v83, v83, v116, 0x43000000
	v_cvt_pk_u8_f32 v82, v83, 1, v82
	v_fmaak_f32 v83, v84, v116, 0x43000000
	v_cvt_pk_u8_f32 v82, v83, 2, v82
	v_fmaak_f32 v83, v85, v116, 0x43000000
	v_cvt_pk_u8_f32 v82, v83, 3, v82
	v_fmaak_f32 v83, v110, v116, 0x43000000
	v_cvt_pk_u8_f32 v83, v83, 0, 0
	v_fmaak_f32 v84, v111, v116, 0x43000000
	v_cvt_pk_u8_f32 v83, v84, 1, v83
	v_fmaak_f32 v84, v112, v116, 0x43000000
	v_cvt_pk_u8_f32 v83, v84, 2, v83
	v_fmaak_f32 v84, v113, v116, 0x43000000
	v_cvt_pk_u8_f32 v83, v84, 3, v83
	ds_write2st64_b64 v108, v[114:115], v[82:83] offset1:5
	v_add_u16_e32 v82, 1, v117
	ds_write_b8 v106, v82 offset:2696
	s_setprio 1
	s_waitcnt lgkmcnt(0)
; DI void phase_edown3(const Ctx& c, int layer) {
;     ...
;         D2_BODY(0, 0, 0); D2_BODY(1, 1, 0);
; #pragma unroll 1
;         for (int J = 2; J < 16; J += 2) { D2_BODY(0, J, 5); D2_BODY(1, J + 1, 0); }
	v_mfma_f32_16x16x32_bf16 v[82:85], v[122:125], v[0:3], 0
	v_mfma_f32_16x16x32_bf16 v[110:113], v[126:129], v[0:3], 0
	v_mfma_f32_16x16x32_bf16 v[114:117], v[122:125], v[32:35], 0
	v_mfma_f32_16x16x32_bf16 v[118:121], v[126:129], v[32:35], 0
	v_mfma_f32_16x16x32_bf16 v[82:85], v[130:133], v[4:7], v[82:85]
	v_mfma_f32_16x16x32_bf16 v[110:113], v[134:137], v[4:7], v[110:113]
	v_mfma_f32_16x16x32_bf16 v[114:117], v[130:133], v[36:39], v[114:117]
	v_mfma_f32_16x16x32_bf16 v[118:121], v[134:137], v[36:39], v[118:121]
	v_mfma_f32_16x16x32_bf16 v[82:85], v[138:141], v[8:11], v[82:85]
	v_mfma_f32_16x16x32_bf16 v[110:113], v[142:145], v[8:11], v[110:113]
	v_mfma_f32_16x16x32_bf16 v[114:117], v[138:141], v[40:43], v[114:117]
	v_mfma_f32_16x16x32_bf16 v[118:121], v[142:145], v[40:43], v[118:121]
	v_mfma_f32_16x16x32_bf16 v[82:85], v[146:149], v[12:15], v[82:85]
	v_mfma_f32_16x16x32_bf16 v[110:113], v[150:153], v[12:15], v[110:113]
	v_mfma_f32_16x16x32_bf16 v[114:117], v[146:149], v[44:47], v[114:117]
	v_mfma_f32_16x16x32_bf16 v[118:121], v[150:153], v[44:47], v[118:121]
	v_mfma_f32_16x16x32_bf16 v[82:85], v[154:157], v[16:19], v[82:85]
	v_mfma_f32_16x16x32_bf16 v[110:113], v[158:161], v[16:19], v[110:113]
	v_mfma_f32_16x16x32_bf16 v[114:117], v[154:157], v[48:51], v[114:117]
	v_mfma_f32_16x16x32_bf16 v[118:121], v[158:161], v[48:51], v[118:121]
	v_mfma_f32_16x16x32_bf16 v[82:85], v[162:165], v[20:23], v[82:85]
	v_mfma_f32_16x16x32_bf16 v[110:113], v[166:169], v[20:23], v[110:113]
	v_mfma_f32_16x16x32_bf16 v[114:117], v[162:165], v[52:55], v[114:117]
	v_mfma_f32_16x16x32_bf16 v[118:121], v[166:169], v[52:55], v[118:121]
	v_mfma_f32_16x16x32_bf16 v[82:85], v[170:173], v[24:27], v[82:85]
	v_mfma_f32_16x16x32_bf16 v[110:113], v[178:181], v[24:27], v[110:113]
	v_mfma_f32_16x16x32_bf16 v[114:117], v[170:173], v[56:59], v[114:117]
	v_mfma_f32_16x16x32_bf16 v[118:121], v[178:181], v[56:59], v[118:121]
	v_mfma_f32_16x16x32_bf16 v[82:85], v[182:185], v[28:31], v[82:85]
	v_mfma_f32_16x16x32_bf16 v[110:113], v[186:189], v[28:31], v[110:113]
	v_mfma_f32_16x16x32_bf16 v[114:117], v[182:185], v[60:63], v[114:117]
	v_mfma_f32_16x16x32_bf16 v[118:121], v[186:189], v[60:63], v[118:121]
	s_setprio 0
	s_nop 3
	v_max_f32_e64 v122, |v83|, |v83|
	v_max_f32_e64 v123, |v82|, |v82|
	v_max_f32_e32 v122, v123, v122
	v_max_f32_e64 v123, |v85|, |v85|
	v_max_f32_e64 v124, |v84|, |v84|
	v_max_f32_e32 v123, v124, v123
	v_max_f32_e64 v124, |v113|, |v113|
	v_max_f32_e64 v125, |v112|, |v112|
	v_max_f32_e32 v124, v125, v124
	v_max3_f32 v124, |v110|, |v111|, v124
	v_max3_f32 v122, v122, v123, v124
	v_mul_f32_e32 v122, 0x3c010204, v122
	v_lshrrev_b32_e32 v123, 23, v122
	v_and_b32_e32 v122, 0x7f800000, v122
	v_sub_u32_e32 v122, 0x7e800000, v122
	v_fmaak_f32 v82, v82, v122, 0x43000000
	v_cvt_pk_u8_f32 v82, v82, 0, 0
	v_fmaak_f32 v83, v83, v122, 0x43000000
	v_cvt_pk_u8_f32 v82, v83, 1, v82
	v_fmaak_f32 v83, v84, v122, 0x43000000
	v_cvt_pk_u8_f32 v82, v83, 2, v82
	v_fmaak_f32 v83, v85, v122, 0x43000000
	v_cvt_pk_u8_f32 v82, v83, 3, v82
	v_fmaak_f32 v83, v110, v122, 0x43000000
	v_cvt_pk_u8_f32 v83, v83, 0, 0
	v_fmaak_f32 v84, v111, v122, 0x43000000
	v_cvt_pk_u8_f32 v83, v84, 1, v83
	v_fmaak_f32 v84, v112, v122, 0x43000000
	v_cvt_pk_u8_f32 v83, v84, 2, v83
	v_fmaak_f32 v84, v113, v122, 0x43000000
	v_cvt_pk_u8_f32 v83, v84, 3, v83
	v_add_u16_e32 v84, 1, v123
	ds_write_b8 v106, v84 offset:140
	v_max_f32_e64 v84, |v115|, |v115|
	v_max_f32_e64 v85, |v114|, |v114|
	v_max_f32_e32 v84, v85, v84
	v_max_f32_e64 v85, |v117|, |v117|
	v_max_f32_e64 v110, |v116|, |v116|
	v_max_f32_e32 v85, v110, v85
	v_max_f32_e64 v110, |v121|, |v121|
	v_max_f32_e64 v111, |v120|, |v120|
	v_max_f32_e32 v110, v111, v110
	v_max3_f32 v110, |v118|, |v119|, v110
	v_max3_f32 v84, v84, v85, v110
	v_mul_f32_e32 v84, 0x3c010204, v84
	v_lshrrev_b32_e32 v110, 23, v84
	v_and_b32_e32 v84, 0x7f800000, v84
	v_sub_u32_e32 v85, 0x7e800000, v84
	v_fmaak_f32 v84, v114, v85, 0x43000000
	v_cvt_pk_u8_f32 v84, v84, 0, 0
	v_fmaak_f32 v111, v115, v85, 0x43000000
	v_cvt_pk_u8_f32 v84, v111, 1, v84
	v_fmaak_f32 v111, v116, v85, 0x43000000
	v_cvt_pk_u8_f32 v84, v111, 2, v84
	v_fmaak_f32 v111, v117, v85, 0x43000000
	v_cvt_pk_u8_f32 v84, v111, 3, v84
	v_fmaak_f32 v111, v118, v85, 0x43000000
	v_cvt_pk_u8_f32 v111, v111, 0, 0
	v_fmaak_f32 v112, v119, v85, 0x43000000
	v_cvt_pk_u8_f32 v111, v112, 1, v111
	v_fmaak_f32 v112, v120, v85, 0x43000000
	v_cvt_pk_u8_f32 v111, v112, 2, v111
	v_fmaak_f32 v85, v121, v85, 0x43000000
	v_cvt_pk_u8_f32 v85, v85, 3, v111
	ds_write2st64_b64 v109, v[82:83], v[84:85] offset1:5
	v_add_u16_e32 v82, 1, v110
	ds_write_b8 v106, v82 offset:2700
	ds_read_b128 v[82:85], v103
	ds_read_b128 v[110:113], v103 offset:1280
	v_lshl_add_u64 v[114:115], s[0:1], 0, v[80:81]
	v_lshl_add_u64 v[118:119], s[0:1], 0, v[78:79]
	s_waitcnt lgkmcnt(0)
	global_store_dwordx4 v[114:115], v[82:85], off nt
	ds_read_b128 v[82:85], v103 offset:2560
	ds_read_b128 v[114:117], v103 offset:3840
	global_store_dwordx4 v[118:119], v[110:113], off nt
	s_nop 1
	v_lshl_add_u64 v[110:111], s[0:1], 0, v[76:77]
	s_waitcnt lgkmcnt(0)
	global_store_dwordx4 v[110:111], v[82:85], off nt
	s_nop 1
	v_lshl_add_u64 v[82:83], s[0:1], 0, v[74:75]
	global_store_dwordx4 v[82:83], v[114:117], off nt
	s_and_saveexec_b64 s[8:9], s[2:3]
	s_cbranch_execz .LBB0_1287
	ds_read_b128 v[82:85], v104 offset:128
	v_lshl_add_u64 v[110:111], s[0:1], 0, v[72:73]
	s_waitcnt lgkmcnt(0)
	global_store_dwordx4 v[110:111], v[82:85], off nt
	s_branch .LBB0_1287
